# v23 + XCD stagger of the GEMM1 unit stream, 1.2 us per XCD
# baseline (speedup 1.0000x reference)
.Lp7_stag:
	s_cmp_eq_u32 s92, 0
	s_cbranch_scc1 .Lp7_stag_done
	s_sleep 45
	s_sub_u32 s92, s92, 1
	s_branch .Lp7_stag
